# epilogue de-serialisation: P7 merge epilogue issues all 16 gate loads up front and consumes them behind one counted vmcnt(15) instead of a load-wait-compute-store ladder
# speedup vs baseline: 1.0265x; 1.0012x over previous
.LBB0_849:
	s_cmp_lg_u32 s31, 0
	v_lshl_add_u32 v4, s56, 8, v1
	s_cselect_b64 s[54:55], -1, 0
	s_lshl_b32 s18, s30, 8
	v_ashrrev_i32_e32 v5, 31, v4
	s_and_b32 s18, s18, 0x700
	v_lshlrev_b64 v[160:161], 12, v[4:5]
	v_or_b32_e32 v154, 16, v4
	v_or_b32_e32 v152, 32, v4
	v_or_b32_e32 v150, 48, v4
	v_lshl_add_u64 v[156:157], s[12:13], 0, v[160:161]
	v_or_b32_e32 v2, s18, v163
	s_and_b64 vcc, exec, s[54:55]
	v_ashrrev_i32_e32 v155, 31, v154
	v_ashrrev_i32_e32 v153, 31, v152
	v_ashrrev_i32_e32 v151, 31, v150
	s_cbranch_vccz .LBB0_857
	v_lshl_add_u64 v[158:159], v[156:157], 0, v[2:3]
	v_add_u32_e32 v212, v160, v2
	global_load_dwordx2 v[180:181], v212, s[12:13] offset:2048
	global_load_dwordx2 v[182:183], v212, s[12:13] offset:2176
	v_add_u32_e32 v213, 0x10000, v212
	global_load_dwordx2 v[184:185], v213, s[12:13] offset:2048
	global_load_dwordx2 v[186:187], v213, s[12:13] offset:2176
	v_add_u32_e32 v213, 0x20000, v212
	global_load_dwordx2 v[188:189], v213, s[12:13] offset:2048
	global_load_dwordx2 v[190:191], v213, s[12:13] offset:2176
	v_add_u32_e32 v213, 0x30000, v212
	global_load_dwordx2 v[192:193], v213, s[12:13] offset:2048
	global_load_dwordx2 v[194:195], v213, s[12:13] offset:2176
	v_add_u32_e32 v213, 0x80000, v212
	global_load_dwordx2 v[196:197], v213, s[12:13] offset:2048
	global_load_dwordx2 v[198:199], v213, s[12:13] offset:2176
	v_add_u32_e32 v213, 0x90000, v212
	global_load_dwordx2 v[200:201], v213, s[12:13] offset:2048
	global_load_dwordx2 v[202:203], v213, s[12:13] offset:2176
	v_add_u32_e32 v213, 0xa0000, v212
	global_load_dwordx2 v[204:205], v213, s[12:13] offset:2048
	global_load_dwordx2 v[206:207], v213, s[12:13] offset:2176
	v_add_u32_e32 v213, 0xb0000, v212
	global_load_dwordx2 v[208:209], v213, s[12:13] offset:2048
	global_load_dwordx2 v[210:211], v213, s[12:13] offset:2176
	s_waitcnt vmcnt(15)
	v_mov_b32_e32 v166, v180
	v_mov_b32_e32 v167, v181
	v_cvt_pk_f32_fp8_e32 v[168:169], v166
	v_cvt_pk_f32_fp8_sdwa v[170:171], v166 src0_sel:WORD_1
	v_cvt_pk_f32_fp8_e32 v[172:173], v167
	v_cvt_pk_f32_fp8_sdwa v[166:167], v167 src0_sel:WORD_1
	v_mul_f32_e32 v165, 0x3d800000, v168
	v_mul_f32_e32 v168, 0x3d800000, v169
	v_mul_f32_e32 v169, 0x3d800000, v170
	v_mul_f32_e32 v170, 0x3d800000, v171
	v_mul_f32_e32 v171, 0x3d800000, v172
	v_mul_f32_e32 v172, 0x3d800000, v173
	v_mul_f32_e32 v166, 0x3d800000, v166
	v_mul_f32_e32 v167, 0x3d800000, v167
	v_mul_f32_e32 v168, 0xbfb8aa3b, v168
	v_mul_f32_e32 v169, 0xbfb8aa3b, v169
	v_mul_f32_e32 v170, 0xbfb8aa3b, v170
	v_mul_f32_e32 v171, 0xbfb8aa3b, v171
	v_mul_f32_e32 v165, 0xbfb8aa3b, v165
	v_mul_f32_e32 v172, 0xbfb8aa3b, v172
	v_mul_f32_e32 v166, 0xbfb8aa3b, v166
	v_mul_f32_e32 v167, 0xbfb8aa3b, v167
	v_exp_f32_e32 v168, v168
	v_exp_f32_e32 v169, v169
	v_exp_f32_e32 v170, v170
	v_exp_f32_e32 v171, v171
	v_exp_f32_e32 v165, v165
	v_exp_f32_e32 v172, v172
	v_exp_f32_e32 v166, v166
	v_exp_f32_e32 v167, v167
	v_add_f32_e32 v168, 1.0, v168
	v_add_f32_e32 v169, 1.0, v169
	v_add_f32_e32 v170, 1.0, v170
	v_add_f32_e32 v171, 1.0, v171
	v_add_f32_e32 v165, 1.0, v165
	v_add_f32_e32 v172, 1.0, v172
	v_add_f32_e32 v166, 1.0, v166
	v_add_f32_e32 v167, 1.0, v167
	v_rcp_f32_e32 v168, v168
	v_rcp_f32_e32 v169, v169
	v_rcp_f32_e32 v170, v170
	v_rcp_f32_e32 v171, v171
	v_rcp_f32_e32 v165, v165
	v_rcp_f32_e32 v172, v172
	v_rcp_f32_e32 v166, v166
	v_rcp_f32_e32 v167, v167
	v_mul_f32_e32 v168, v131, v168
	v_mul_f32_e32 v169, v132, v169
	v_mul_f32_e32 v170, v133, v170
	v_mul_f32_e32 v171, v126, v171
	v_mul_f32_e32 v165, v130, v165
	v_mul_f32_e32 v172, v127, v172
	v_mul_f32_e32 v173, v128, v166
	v_mul_f32_e32 v174, v129, v167
	v_cvt_pk_bf16_f32 v166, v165, v168
	v_cvt_pk_bf16_f32 v167, v169, v170
	v_cvt_pk_bf16_f32 v168, v171, v172
	v_cvt_pk_bf16_f32 v169, v173, v174
	v_lshl_add_u64 v[172:173], s[10:11], 0, v[160:161]
	v_lshlrev_b32_e32 v158, 1, v2
	v_mov_b32_e32 v159, v3
	v_lshl_add_u64 v[172:173], v[172:173], 0, v[158:159]
	global_store_dwordx4 v[172:173], v[166:169], off
	v_lshlrev_b64 v[174:175], 12, v[154:155]
	v_lshl_add_u64 v[176:177], s[12:13], 0, v[174:175]
	v_lshl_add_u64 v[176:177], v[176:177], 0, v[2:3]
	v_lshl_add_u64 v[174:175], s[10:11], 0, v[174:175]
	v_lshl_add_u64 v[174:175], v[174:175], 0, v[158:159]
	s_waitcnt vmcnt(15)
	v_mov_b32_e32 v170, v182
	v_mov_b32_e32 v171, v183
	v_cvt_pk_f32_fp8_e32 v[166:167], v170
	v_cvt_pk_f32_fp8_sdwa v[168:169], v170 src0_sel:WORD_1
	v_cvt_pk_f32_fp8_e32 v[178:179], v171
	v_cvt_pk_f32_fp8_sdwa v[170:171], v171 src0_sel:WORD_1
	v_mul_f32_e32 v165, 0x3d800000, v166
	v_mul_f32_e32 v166, 0x3d800000, v167
	v_mul_f32_e32 v167, 0x3d800000, v168
	v_mul_f32_e32 v168, 0x3d800000, v169
	v_mul_f32_e32 v169, 0x3d800000, v178
	v_mul_f32_e32 v170, 0x3d800000, v170
	v_mul_f32_e32 v171, 0x3d800000, v171
	v_mul_f32_e32 v178, 0x3d800000, v179
	v_mul_f32_e32 v166, 0xbfb8aa3b, v166
	v_mul_f32_e32 v167, 0xbfb8aa3b, v167
	v_mul_f32_e32 v168, 0xbfb8aa3b, v168
	v_mul_f32_e32 v169, 0xbfb8aa3b, v169
	v_mul_f32_e32 v170, 0xbfb8aa3b, v170
	v_mul_f32_e32 v171, 0xbfb8aa3b, v171
	v_mul_f32_e32 v165, 0xbfb8aa3b, v165
	v_mul_f32_e32 v178, 0xbfb8aa3b, v178
	v_exp_f32_e32 v166, v166
	v_exp_f32_e32 v167, v167
	v_exp_f32_e32 v168, v168
	v_exp_f32_e32 v169, v169
	v_exp_f32_e32 v170, v170
	v_exp_f32_e32 v171, v171
	v_exp_f32_e32 v165, v165
	v_exp_f32_e32 v178, v178
	v_add_f32_e32 v166, 1.0, v166
	v_add_f32_e32 v167, 1.0, v167
	v_add_f32_e32 v168, 1.0, v168
	v_add_f32_e32 v169, 1.0, v169
	v_add_f32_e32 v170, 1.0, v170
	v_add_f32_e32 v171, 1.0, v171
	v_add_f32_e32 v165, 1.0, v165
	v_add_f32_e32 v178, 1.0, v178
	v_rcp_f32_e32 v166, v166
	v_rcp_f32_e32 v167, v167
	v_rcp_f32_e32 v168, v168
	v_rcp_f32_e32 v169, v169
	v_rcp_f32_e32 v170, v170
	v_rcp_f32_e32 v171, v171
	v_rcp_f32_e32 v165, v165
	v_rcp_f32_e32 v178, v178
	v_mul_f32_e32 v166, v99, v166
	v_mul_f32_e32 v167, v100, v167
	v_mul_f32_e32 v168, v101, v168
	v_mul_f32_e32 v169, v94, v169
	v_mul_f32_e32 v170, v96, v170
	v_mul_f32_e32 v171, v97, v171
	v_mul_f32_e32 v165, v98, v165
	v_mul_f32_e32 v178, v95, v178
	v_cvt_pk_bf16_f32 v166, v165, v166
	v_cvt_pk_bf16_f32 v167, v167, v168
	v_cvt_pk_bf16_f32 v168, v169, v178
	v_cvt_pk_bf16_f32 v169, v170, v171
	s_nop 0
	global_store_dwordx4 v[172:173], v[166:169], off offset:256
	s_waitcnt vmcnt(15)
	v_mov_b32_e32 v170, v184
	v_mov_b32_e32 v171, v185
	v_cvt_pk_f32_fp8_e32 v[172:173], v171
	v_cvt_pk_f32_fp8_e32 v[166:167], v170
	v_cvt_pk_f32_fp8_sdwa v[168:169], v170 src0_sel:WORD_1
	v_cvt_pk_f32_fp8_sdwa v[170:171], v171 src0_sel:WORD_1
	v_mul_f32_e32 v165, 0x3d800000, v166
	v_mul_f32_e32 v166, 0x3d800000, v167
	v_mul_f32_e32 v167, 0x3d800000, v168
	v_mul_f32_e32 v168, 0x3d800000, v169
	v_mul_f32_e32 v169, 0x3d800000, v172
	v_mul_f32_e32 v170, 0x3d800000, v170
	v_mul_f32_e32 v171, 0x3d800000, v171
	v_mul_f32_e32 v172, 0x3d800000, v173
	v_mul_f32_e32 v166, 0xbfb8aa3b, v166
	v_mul_f32_e32 v167, 0xbfb8aa3b, v167
	v_mul_f32_e32 v168, 0xbfb8aa3b, v168
	v_mul_f32_e32 v169, 0xbfb8aa3b, v169
	v_mul_f32_e32 v170, 0xbfb8aa3b, v170
	v_mul_f32_e32 v171, 0xbfb8aa3b, v171
	v_mul_f32_e32 v165, 0xbfb8aa3b, v165
	v_mul_f32_e32 v172, 0xbfb8aa3b, v172
	v_exp_f32_e32 v166, v166
	v_exp_f32_e32 v167, v167
	v_exp_f32_e32 v168, v168
	v_exp_f32_e32 v169, v169
	v_exp_f32_e32 v170, v170
	v_exp_f32_e32 v171, v171
	v_exp_f32_e32 v165, v165
	v_exp_f32_e32 v172, v172
	v_add_f32_e32 v166, 1.0, v166
	v_add_f32_e32 v167, 1.0, v167
	v_add_f32_e32 v168, 1.0, v168
	v_add_f32_e32 v169, 1.0, v169
	v_add_f32_e32 v170, 1.0, v170
	v_add_f32_e32 v171, 1.0, v171
	v_add_f32_e32 v165, 1.0, v165
	v_add_f32_e32 v172, 1.0, v172
	v_rcp_f32_e32 v166, v166
	v_rcp_f32_e32 v167, v167
	v_rcp_f32_e32 v168, v168
	v_rcp_f32_e32 v169, v169
	v_rcp_f32_e32 v170, v170
	v_rcp_f32_e32 v171, v171
	v_rcp_f32_e32 v165, v165
	v_rcp_f32_e32 v172, v172
	v_mul_f32_e32 v166, v123, v166
	v_mul_f32_e32 v167, v124, v167
	v_mul_f32_e32 v168, v125, v168
	v_mul_f32_e32 v169, v118, v169
	v_mul_f32_e32 v170, v120, v170
	v_mul_f32_e32 v171, v121, v171
	v_mul_f32_e32 v165, v122, v165
	v_mul_f32_e32 v172, v119, v172
	v_cvt_pk_bf16_f32 v166, v165, v166
	v_cvt_pk_bf16_f32 v167, v167, v168
	v_cvt_pk_bf16_f32 v168, v169, v172
	v_cvt_pk_bf16_f32 v169, v170, v171
	v_lshlrev_b64 v[172:173], 12, v[152:153]
	global_store_dwordx4 v[174:175], v[166:169], off
	v_lshl_add_u64 v[176:177], s[12:13], 0, v[172:173]
	v_lshl_add_u64 v[176:177], v[176:177], 0, v[2:3]
	v_lshl_add_u64 v[172:173], s[10:11], 0, v[172:173]
	v_lshl_add_u64 v[172:173], v[172:173], 0, v[158:159]
	s_waitcnt vmcnt(15)
	v_mov_b32_e32 v170, v186
	v_mov_b32_e32 v171, v187
	v_cvt_pk_f32_fp8_e32 v[166:167], v170
	v_cvt_pk_f32_fp8_sdwa v[168:169], v170 src0_sel:WORD_1
	v_cvt_pk_f32_fp8_e32 v[178:179], v171
	v_cvt_pk_f32_fp8_sdwa v[170:171], v171 src0_sel:WORD_1
	v_mul_f32_e32 v165, 0x3d800000, v166
	v_mul_f32_e32 v166, 0x3d800000, v167
	v_mul_f32_e32 v167, 0x3d800000, v168
	v_mul_f32_e32 v168, 0x3d800000, v169
	v_mul_f32_e32 v169, 0x3d800000, v178
	v_mul_f32_e32 v170, 0x3d800000, v170
	v_mul_f32_e32 v171, 0x3d800000, v171
	v_mul_f32_e32 v178, 0x3d800000, v179
	v_mul_f32_e32 v166, 0xbfb8aa3b, v166
	v_mul_f32_e32 v167, 0xbfb8aa3b, v167
	v_mul_f32_e32 v168, 0xbfb8aa3b, v168
	v_mul_f32_e32 v169, 0xbfb8aa3b, v169
	v_mul_f32_e32 v170, 0xbfb8aa3b, v170
	v_mul_f32_e32 v171, 0xbfb8aa3b, v171
	v_mul_f32_e32 v165, 0xbfb8aa3b, v165
	v_mul_f32_e32 v178, 0xbfb8aa3b, v178
	v_exp_f32_e32 v166, v166
	v_exp_f32_e32 v167, v167
	v_exp_f32_e32 v168, v168
	v_exp_f32_e32 v169, v169
	v_exp_f32_e32 v170, v170
	v_exp_f32_e32 v171, v171
	v_exp_f32_e32 v165, v165
	v_exp_f32_e32 v178, v178
	v_add_f32_e32 v166, 1.0, v166
	v_add_f32_e32 v167, 1.0, v167
	v_add_f32_e32 v168, 1.0, v168
	v_add_f32_e32 v169, 1.0, v169
	v_add_f32_e32 v170, 1.0, v170
	v_add_f32_e32 v171, 1.0, v171
	v_add_f32_e32 v165, 1.0, v165
	v_add_f32_e32 v178, 1.0, v178
	v_rcp_f32_e32 v166, v166
	v_rcp_f32_e32 v167, v167
	v_rcp_f32_e32 v168, v168
	v_rcp_f32_e32 v169, v169
	v_rcp_f32_e32 v170, v170
	v_rcp_f32_e32 v171, v171
	v_rcp_f32_e32 v165, v165
	v_rcp_f32_e32 v178, v178
	v_mul_f32_e32 v166, v91, v166
	v_mul_f32_e32 v167, v92, v167
	v_mul_f32_e32 v168, v93, v168
	v_mul_f32_e32 v169, v86, v169
	v_mul_f32_e32 v170, v88, v170
	v_mul_f32_e32 v171, v89, v171
	v_mul_f32_e32 v165, v90, v165
	v_mul_f32_e32 v178, v87, v178
	v_cvt_pk_bf16_f32 v166, v165, v166
	v_cvt_pk_bf16_f32 v167, v167, v168
	v_cvt_pk_bf16_f32 v168, v169, v178
	v_cvt_pk_bf16_f32 v169, v170, v171
	s_nop 0
	global_store_dwordx4 v[174:175], v[166:169], off offset:256
	s_waitcnt vmcnt(15)
	v_mov_b32_e32 v170, v188
	v_mov_b32_e32 v171, v189
	v_cvt_pk_f32_fp8_e32 v[174:175], v171
	v_cvt_pk_f32_fp8_e32 v[166:167], v170
	v_cvt_pk_f32_fp8_sdwa v[168:169], v170 src0_sel:WORD_1
	v_cvt_pk_f32_fp8_sdwa v[170:171], v171 src0_sel:WORD_1
	v_mul_f32_e32 v165, 0x3d800000, v166
	v_mul_f32_e32 v166, 0x3d800000, v167
	v_mul_f32_e32 v167, 0x3d800000, v168
	v_mul_f32_e32 v168, 0x3d800000, v169
	v_mul_f32_e32 v169, 0x3d800000, v174
	v_mul_f32_e32 v170, 0x3d800000, v170
	v_mul_f32_e32 v171, 0x3d800000, v171
	v_mul_f32_e32 v174, 0x3d800000, v175
	v_mul_f32_e32 v166, 0xbfb8aa3b, v166
	v_mul_f32_e32 v167, 0xbfb8aa3b, v167
	v_mul_f32_e32 v168, 0xbfb8aa3b, v168
	v_mul_f32_e32 v169, 0xbfb8aa3b, v169
	v_mul_f32_e32 v170, 0xbfb8aa3b, v170
	v_mul_f32_e32 v171, 0xbfb8aa3b, v171
	v_mul_f32_e32 v165, 0xbfb8aa3b, v165
	v_mul_f32_e32 v174, 0xbfb8aa3b, v174
	v_exp_f32_e32 v166, v166
	v_exp_f32_e32 v167, v167
	v_exp_f32_e32 v168, v168
	v_exp_f32_e32 v169, v169
	v_exp_f32_e32 v170, v170
	v_exp_f32_e32 v171, v171
	v_exp_f32_e32 v165, v165
	v_exp_f32_e32 v174, v174
	v_add_f32_e32 v166, 1.0, v166
	v_add_f32_e32 v167, 1.0, v167
	v_add_f32_e32 v168, 1.0, v168
	v_add_f32_e32 v169, 1.0, v169
	v_add_f32_e32 v170, 1.0, v170
	v_add_f32_e32 v171, 1.0, v171
	v_add_f32_e32 v165, 1.0, v165
	v_add_f32_e32 v174, 1.0, v174
	v_rcp_f32_e32 v166, v166
	v_rcp_f32_e32 v167, v167
	v_rcp_f32_e32 v168, v168
	v_rcp_f32_e32 v169, v169
	v_rcp_f32_e32 v170, v170
	v_rcp_f32_e32 v171, v171
	v_rcp_f32_e32 v165, v165
	v_rcp_f32_e32 v174, v174
	v_mul_f32_e32 v166, v115, v166
	v_mul_f32_e32 v167, v116, v167
	v_mul_f32_e32 v168, v117, v168
	v_mul_f32_e32 v169, v110, v169
	v_mul_f32_e32 v170, v112, v170
	v_mul_f32_e32 v171, v113, v171
	v_mul_f32_e32 v165, v114, v165
	v_mul_f32_e32 v174, v111, v174
	v_cvt_pk_bf16_f32 v166, v165, v166
	v_cvt_pk_bf16_f32 v167, v167, v168
	v_cvt_pk_bf16_f32 v168, v169, v174
	v_cvt_pk_bf16_f32 v169, v170, v171
	v_lshlrev_b64 v[174:175], 12, v[150:151]
	global_store_dwordx4 v[172:173], v[166:169], off
	v_lshl_add_u64 v[176:177], s[12:13], 0, v[174:175]
	v_lshl_add_u64 v[176:177], v[176:177], 0, v[2:3]
	v_lshl_add_u64 v[174:175], s[10:11], 0, v[174:175]
	v_lshl_add_u64 v[174:175], v[174:175], 0, v[158:159]
	s_waitcnt vmcnt(15)
	v_mov_b32_e32 v170, v190
	v_mov_b32_e32 v171, v191
	v_cvt_pk_f32_fp8_e32 v[166:167], v170
	v_cvt_pk_f32_fp8_sdwa v[168:169], v170 src0_sel:WORD_1
	v_cvt_pk_f32_fp8_e32 v[178:179], v171
	v_cvt_pk_f32_fp8_sdwa v[170:171], v171 src0_sel:WORD_1
	v_mul_f32_e32 v165, 0x3d800000, v166
	v_mul_f32_e32 v166, 0x3d800000, v167
	v_mul_f32_e32 v167, 0x3d800000, v168
	v_mul_f32_e32 v168, 0x3d800000, v169
	v_mul_f32_e32 v169, 0x3d800000, v178
	v_mul_f32_e32 v170, 0x3d800000, v170
	v_mul_f32_e32 v171, 0x3d800000, v171
	v_mul_f32_e32 v178, 0x3d800000, v179
	v_mul_f32_e32 v166, 0xbfb8aa3b, v166
	v_mul_f32_e32 v167, 0xbfb8aa3b, v167
	v_mul_f32_e32 v168, 0xbfb8aa3b, v168
	v_mul_f32_e32 v169, 0xbfb8aa3b, v169
	v_mul_f32_e32 v170, 0xbfb8aa3b, v170
	v_mul_f32_e32 v171, 0xbfb8aa3b, v171
	v_mul_f32_e32 v165, 0xbfb8aa3b, v165
	v_mul_f32_e32 v178, 0xbfb8aa3b, v178
	v_exp_f32_e32 v166, v166
	v_exp_f32_e32 v167, v167
	v_exp_f32_e32 v168, v168
	v_exp_f32_e32 v169, v169
	v_exp_f32_e32 v170, v170
	v_exp_f32_e32 v171, v171
	v_exp_f32_e32 v165, v165
	v_exp_f32_e32 v178, v178
	v_add_f32_e32 v166, 1.0, v166
	v_add_f32_e32 v167, 1.0, v167
	v_add_f32_e32 v168, 1.0, v168
	v_add_f32_e32 v169, 1.0, v169
	v_add_f32_e32 v170, 1.0, v170
	v_add_f32_e32 v171, 1.0, v171
	v_add_f32_e32 v165, 1.0, v165
	v_add_f32_e32 v178, 1.0, v178
	v_rcp_f32_e32 v166, v166
	v_rcp_f32_e32 v167, v167
	v_rcp_f32_e32 v168, v168
	v_rcp_f32_e32 v169, v169
	v_rcp_f32_e32 v170, v170
	v_rcp_f32_e32 v171, v171
	v_rcp_f32_e32 v165, v165
	v_rcp_f32_e32 v178, v178
	v_mul_f32_e32 v166, v83, v166
	v_mul_f32_e32 v167, v84, v167
	v_mul_f32_e32 v168, v85, v168
	v_mul_f32_e32 v169, v78, v169
	v_mul_f32_e32 v170, v80, v170
	v_mul_f32_e32 v171, v81, v171
	v_mul_f32_e32 v165, v82, v165
	v_mul_f32_e32 v178, v79, v178
	v_cvt_pk_bf16_f32 v166, v165, v166
	v_cvt_pk_bf16_f32 v167, v167, v168
	v_cvt_pk_bf16_f32 v168, v169, v178
	v_cvt_pk_bf16_f32 v169, v170, v171
	s_nop 0
	global_store_dwordx4 v[172:173], v[166:169], off offset:256
	s_waitcnt vmcnt(15)
	v_mov_b32_e32 v170, v192
	v_mov_b32_e32 v171, v193
	v_cvt_pk_f32_fp8_e32 v[172:173], v171
	v_cvt_pk_f32_fp8_e32 v[166:167], v170
	v_cvt_pk_f32_fp8_sdwa v[168:169], v170 src0_sel:WORD_1
	v_cvt_pk_f32_fp8_sdwa v[170:171], v171 src0_sel:WORD_1
	v_mul_f32_e32 v165, 0x3d800000, v166
	v_mul_f32_e32 v166, 0x3d800000, v167
	v_mul_f32_e32 v167, 0x3d800000, v168
	v_mul_f32_e32 v168, 0x3d800000, v169
	v_mul_f32_e32 v169, 0x3d800000, v172
	v_mul_f32_e32 v170, 0x3d800000, v170
	v_mul_f32_e32 v171, 0x3d800000, v171
	v_mul_f32_e32 v172, 0x3d800000, v173
	v_mul_f32_e32 v166, 0xbfb8aa3b, v166
	v_mul_f32_e32 v167, 0xbfb8aa3b, v167
	v_mul_f32_e32 v168, 0xbfb8aa3b, v168
	v_mul_f32_e32 v169, 0xbfb8aa3b, v169
	v_mul_f32_e32 v170, 0xbfb8aa3b, v170
	v_mul_f32_e32 v171, 0xbfb8aa3b, v171
	v_mul_f32_e32 v165, 0xbfb8aa3b, v165
	v_mul_f32_e32 v172, 0xbfb8aa3b, v172
	v_exp_f32_e32 v166, v166
	v_exp_f32_e32 v167, v167
	v_exp_f32_e32 v168, v168
	v_exp_f32_e32 v169, v169
	v_exp_f32_e32 v170, v170
	v_exp_f32_e32 v171, v171
	v_exp_f32_e32 v165, v165
	v_exp_f32_e32 v172, v172
	v_add_f32_e32 v166, 1.0, v166
	v_add_f32_e32 v167, 1.0, v167
	v_add_f32_e32 v168, 1.0, v168
	v_add_f32_e32 v169, 1.0, v169
	v_add_f32_e32 v170, 1.0, v170
	v_add_f32_e32 v171, 1.0, v171
	v_add_f32_e32 v165, 1.0, v165
	v_add_f32_e32 v172, 1.0, v172
	v_rcp_f32_e32 v166, v166
	v_rcp_f32_e32 v167, v167
	v_rcp_f32_e32 v168, v168
	v_rcp_f32_e32 v169, v169
	v_rcp_f32_e32 v170, v170
	v_rcp_f32_e32 v171, v171
	v_rcp_f32_e32 v165, v165
	v_rcp_f32_e32 v172, v172
	v_mul_f32_e32 v166, v107, v166
	v_mul_f32_e32 v167, v108, v167
	v_mul_f32_e32 v168, v109, v168
	v_mul_f32_e32 v169, v102, v169
	v_mul_f32_e32 v170, v104, v170
	v_mul_f32_e32 v171, v105, v171
	v_mul_f32_e32 v165, v106, v165
	v_mul_f32_e32 v172, v103, v172
	v_cvt_pk_bf16_f32 v166, v165, v166
	v_cvt_pk_bf16_f32 v167, v167, v168
	v_cvt_pk_bf16_f32 v168, v169, v172
	v_cvt_pk_bf16_f32 v169, v170, v171
	v_lshl_add_u64 v[172:173], v[160:161], 0, s[0:1]
	global_store_dwordx4 v[174:175], v[166:169], off
	v_lshl_add_u64 v[176:177], s[12:13], 0, v[172:173]
	v_lshl_add_u64 v[176:177], v[176:177], 0, v[2:3]
	v_lshl_add_u64 v[172:173], s[10:11], 0, v[172:173]
	v_lshl_add_u64 v[172:173], v[172:173], 0, v[158:159]
	s_waitcnt vmcnt(15)
	v_mov_b32_e32 v170, v194
	v_mov_b32_e32 v171, v195
	v_cvt_pk_f32_fp8_e32 v[166:167], v170
	v_cvt_pk_f32_fp8_sdwa v[168:169], v170 src0_sel:WORD_1
	v_cvt_pk_f32_fp8_e32 v[178:179], v171
	v_cvt_pk_f32_fp8_sdwa v[170:171], v171 src0_sel:WORD_1
	v_mul_f32_e32 v165, 0x3d800000, v166
	v_mul_f32_e32 v166, 0x3d800000, v167
	v_mul_f32_e32 v167, 0x3d800000, v168
	v_mul_f32_e32 v168, 0x3d800000, v169
	v_mul_f32_e32 v169, 0x3d800000, v178
	v_mul_f32_e32 v170, 0x3d800000, v170
	v_mul_f32_e32 v171, 0x3d800000, v171
	v_mul_f32_e32 v178, 0x3d800000, v179
	v_mul_f32_e32 v166, 0xbfb8aa3b, v166
	v_mul_f32_e32 v167, 0xbfb8aa3b, v167
	v_mul_f32_e32 v168, 0xbfb8aa3b, v168
	v_mul_f32_e32 v169, 0xbfb8aa3b, v169
	v_mul_f32_e32 v170, 0xbfb8aa3b, v170
	v_mul_f32_e32 v171, 0xbfb8aa3b, v171
	v_mul_f32_e32 v165, 0xbfb8aa3b, v165
	v_mul_f32_e32 v178, 0xbfb8aa3b, v178
	v_exp_f32_e32 v166, v166
	v_exp_f32_e32 v167, v167
	v_exp_f32_e32 v168, v168
	v_exp_f32_e32 v169, v169
	v_exp_f32_e32 v170, v170
	v_exp_f32_e32 v171, v171
	v_exp_f32_e32 v165, v165
	v_exp_f32_e32 v178, v178
	v_add_f32_e32 v166, 1.0, v166
	v_add_f32_e32 v167, 1.0, v167
	v_add_f32_e32 v168, 1.0, v168
	v_add_f32_e32 v169, 1.0, v169
	v_add_f32_e32 v170, 1.0, v170
	v_add_f32_e32 v171, 1.0, v171
	v_add_f32_e32 v165, 1.0, v165
	v_add_f32_e32 v178, 1.0, v178
	v_rcp_f32_e32 v166, v166
	v_rcp_f32_e32 v167, v167
	v_rcp_f32_e32 v168, v168
	v_rcp_f32_e32 v169, v169
	v_rcp_f32_e32 v170, v170
	v_rcp_f32_e32 v171, v171
	v_rcp_f32_e32 v165, v165
	v_rcp_f32_e32 v178, v178
	v_mul_f32_e32 v166, v75, v166
	v_mul_f32_e32 v167, v76, v167
	v_mul_f32_e32 v168, v77, v168
	v_mul_f32_e32 v169, v70, v169
	v_mul_f32_e32 v170, v72, v170
	v_mul_f32_e32 v171, v73, v171
	v_mul_f32_e32 v165, v74, v165
	v_mul_f32_e32 v178, v71, v178
	v_cvt_pk_bf16_f32 v166, v165, v166
	v_cvt_pk_bf16_f32 v167, v167, v168
	v_cvt_pk_bf16_f32 v168, v169, v178
	v_cvt_pk_bf16_f32 v169, v170, v171
	s_nop 0
	global_store_dwordx4 v[174:175], v[166:169], off offset:256
	s_waitcnt vmcnt(15)
	v_mov_b32_e32 v170, v196
	v_mov_b32_e32 v171, v197
	v_cvt_pk_f32_fp8_e32 v[174:175], v171
	v_cvt_pk_f32_fp8_e32 v[166:167], v170
	v_cvt_pk_f32_fp8_sdwa v[168:169], v170 src0_sel:WORD_1
	v_cvt_pk_f32_fp8_sdwa v[170:171], v171 src0_sel:WORD_1
	v_mul_f32_e32 v165, 0x3d800000, v166
	v_mul_f32_e32 v166, 0x3d800000, v167
	v_mul_f32_e32 v167, 0x3d800000, v168
	v_mul_f32_e32 v168, 0x3d800000, v169
	v_mul_f32_e32 v169, 0x3d800000, v174
	v_mul_f32_e32 v170, 0x3d800000, v170
	v_mul_f32_e32 v171, 0x3d800000, v171
	v_mul_f32_e32 v174, 0x3d800000, v175
	v_mul_f32_e32 v166, 0xbfb8aa3b, v166
	v_mul_f32_e32 v167, 0xbfb8aa3b, v167
	v_mul_f32_e32 v168, 0xbfb8aa3b, v168
	v_mul_f32_e32 v169, 0xbfb8aa3b, v169
	v_mul_f32_e32 v170, 0xbfb8aa3b, v170
	v_mul_f32_e32 v171, 0xbfb8aa3b, v171
	v_mul_f32_e32 v165, 0xbfb8aa3b, v165
	v_mul_f32_e32 v174, 0xbfb8aa3b, v174
	v_exp_f32_e32 v166, v166
	v_exp_f32_e32 v167, v167
	v_exp_f32_e32 v168, v168
	v_exp_f32_e32 v169, v169
	v_exp_f32_e32 v170, v170
	v_exp_f32_e32 v171, v171
	v_exp_f32_e32 v165, v165
	v_exp_f32_e32 v174, v174
	v_add_f32_e32 v166, 1.0, v166
	v_add_f32_e32 v167, 1.0, v167
	v_add_f32_e32 v168, 1.0, v168
	v_add_f32_e32 v169, 1.0, v169
	v_add_f32_e32 v170, 1.0, v170
	v_add_f32_e32 v171, 1.0, v171
	v_add_f32_e32 v165, 1.0, v165
	v_add_f32_e32 v174, 1.0, v174
	v_rcp_f32_e32 v166, v166
	v_rcp_f32_e32 v167, v167
	v_rcp_f32_e32 v168, v168
	v_rcp_f32_e32 v169, v169
	v_rcp_f32_e32 v170, v170
	v_rcp_f32_e32 v171, v171
	v_rcp_f32_e32 v165, v165
	v_rcp_f32_e32 v174, v174
	v_mul_f32_e32 v166, v67, v166
	v_mul_f32_e32 v167, v68, v167
	v_mul_f32_e32 v168, v69, v168
	v_mul_f32_e32 v169, v62, v169
	v_mul_f32_e32 v170, v64, v170
	v_mul_f32_e32 v171, v65, v171
	v_mul_f32_e32 v165, v66, v165
	v_mul_f32_e32 v174, v63, v174
	v_cvt_pk_bf16_f32 v166, v165, v166
	v_cvt_pk_bf16_f32 v167, v167, v168
	v_cvt_pk_bf16_f32 v168, v169, v174
	v_cvt_pk_bf16_f32 v169, v170, v171
	v_lshl_add_u64 v[174:175], v[160:161], 0, s[38:39]
	global_store_dwordx4 v[172:173], v[166:169], off
	v_lshl_add_u64 v[176:177], s[12:13], 0, v[174:175]
	v_lshl_add_u64 v[176:177], v[176:177], 0, v[2:3]
	v_lshl_add_u64 v[174:175], s[10:11], 0, v[174:175]
	v_lshl_add_u64 v[174:175], v[174:175], 0, v[158:159]
	s_waitcnt vmcnt(15)
	v_mov_b32_e32 v170, v198
	v_mov_b32_e32 v171, v199
	v_cvt_pk_f32_fp8_e32 v[166:167], v170
	v_cvt_pk_f32_fp8_sdwa v[168:169], v170 src0_sel:WORD_1
	v_cvt_pk_f32_fp8_e32 v[178:179], v171
	v_cvt_pk_f32_fp8_sdwa v[170:171], v171 src0_sel:WORD_1
	v_mul_f32_e32 v165, 0x3d800000, v166
	v_mul_f32_e32 v166, 0x3d800000, v167
	v_mul_f32_e32 v167, 0x3d800000, v168
	v_mul_f32_e32 v168, 0x3d800000, v169
	v_mul_f32_e32 v169, 0x3d800000, v178
	v_mul_f32_e32 v170, 0x3d800000, v170
	v_mul_f32_e32 v171, 0x3d800000, v171
	v_mul_f32_e32 v178, 0x3d800000, v179
	v_mul_f32_e32 v166, 0xbfb8aa3b, v166
	v_mul_f32_e32 v167, 0xbfb8aa3b, v167
	v_mul_f32_e32 v168, 0xbfb8aa3b, v168
	v_mul_f32_e32 v169, 0xbfb8aa3b, v169
	v_mul_f32_e32 v170, 0xbfb8aa3b, v170
	v_mul_f32_e32 v171, 0xbfb8aa3b, v171
	v_mul_f32_e32 v165, 0xbfb8aa3b, v165
	v_mul_f32_e32 v178, 0xbfb8aa3b, v178
	v_exp_f32_e32 v166, v166
	v_exp_f32_e32 v167, v167
	v_exp_f32_e32 v168, v168
	v_exp_f32_e32 v169, v169
	v_exp_f32_e32 v170, v170
	v_exp_f32_e32 v171, v171
	v_exp_f32_e32 v165, v165
	v_exp_f32_e32 v178, v178
	v_add_f32_e32 v166, 1.0, v166
	v_add_f32_e32 v167, 1.0, v167
	v_add_f32_e32 v168, 1.0, v168
	v_add_f32_e32 v169, 1.0, v169
	v_add_f32_e32 v170, 1.0, v170
	v_add_f32_e32 v171, 1.0, v171
	v_add_f32_e32 v165, 1.0, v165
	v_add_f32_e32 v178, 1.0, v178
	v_rcp_f32_e32 v166, v166
	v_rcp_f32_e32 v167, v167
	v_rcp_f32_e32 v168, v168
	v_rcp_f32_e32 v169, v169
	v_rcp_f32_e32 v170, v170
	v_rcp_f32_e32 v171, v171
	v_rcp_f32_e32 v165, v165
	v_rcp_f32_e32 v178, v178
	v_mul_f32_e32 v166, v35, v166
	v_mul_f32_e32 v167, v36, v167
	v_mul_f32_e32 v168, v37, v168
	v_mul_f32_e32 v169, v30, v169
	v_mul_f32_e32 v170, v32, v170
	v_mul_f32_e32 v171, v33, v171
	v_mul_f32_e32 v165, v34, v165
	v_mul_f32_e32 v178, v31, v178
	v_cvt_pk_bf16_f32 v166, v165, v166
	v_cvt_pk_bf16_f32 v167, v167, v168
	v_cvt_pk_bf16_f32 v168, v169, v178
	v_cvt_pk_bf16_f32 v169, v170, v171
	s_nop 0
	global_store_dwordx4 v[172:173], v[166:169], off offset:256
	s_waitcnt vmcnt(15)
	v_mov_b32_e32 v170, v200
	v_mov_b32_e32 v171, v201
	v_cvt_pk_f32_fp8_e32 v[172:173], v171
	v_cvt_pk_f32_fp8_e32 v[166:167], v170
	v_cvt_pk_f32_fp8_sdwa v[168:169], v170 src0_sel:WORD_1
	v_cvt_pk_f32_fp8_sdwa v[170:171], v171 src0_sel:WORD_1
	v_mul_f32_e32 v165, 0x3d800000, v166
	v_mul_f32_e32 v166, 0x3d800000, v167
	v_mul_f32_e32 v167, 0x3d800000, v168
	v_mul_f32_e32 v168, 0x3d800000, v169
	v_mul_f32_e32 v169, 0x3d800000, v172
	v_mul_f32_e32 v170, 0x3d800000, v170
	v_mul_f32_e32 v171, 0x3d800000, v171
	v_mul_f32_e32 v172, 0x3d800000, v173
	v_mul_f32_e32 v166, 0xbfb8aa3b, v166
	v_mul_f32_e32 v167, 0xbfb8aa3b, v167
	v_mul_f32_e32 v168, 0xbfb8aa3b, v168
	v_mul_f32_e32 v169, 0xbfb8aa3b, v169
	v_mul_f32_e32 v170, 0xbfb8aa3b, v170
	v_mul_f32_e32 v171, 0xbfb8aa3b, v171
	v_mul_f32_e32 v165, 0xbfb8aa3b, v165
	v_mul_f32_e32 v172, 0xbfb8aa3b, v172
	v_exp_f32_e32 v166, v166
	v_exp_f32_e32 v167, v167
	v_exp_f32_e32 v168, v168
	v_exp_f32_e32 v169, v169
	v_exp_f32_e32 v170, v170
	v_exp_f32_e32 v171, v171
	v_exp_f32_e32 v165, v165
	v_exp_f32_e32 v172, v172
	v_add_f32_e32 v166, 1.0, v166
	v_add_f32_e32 v167, 1.0, v167
	v_add_f32_e32 v168, 1.0, v168
	v_add_f32_e32 v169, 1.0, v169
	v_add_f32_e32 v170, 1.0, v170
	v_add_f32_e32 v171, 1.0, v171
	v_add_f32_e32 v165, 1.0, v165
	v_add_f32_e32 v172, 1.0, v172
	v_rcp_f32_e32 v166, v166
	v_rcp_f32_e32 v167, v167
	v_rcp_f32_e32 v168, v168
	v_rcp_f32_e32 v169, v169
	v_rcp_f32_e32 v170, v170
	v_rcp_f32_e32 v171, v171
	v_rcp_f32_e32 v165, v165
	v_rcp_f32_e32 v172, v172
	v_mul_f32_e32 v166, v59, v166
	v_mul_f32_e32 v167, v60, v167
	v_mul_f32_e32 v168, v61, v168
	v_mul_f32_e32 v169, v54, v169
	v_mul_f32_e32 v170, v56, v170
	v_mul_f32_e32 v171, v57, v171
	v_mul_f32_e32 v165, v58, v165
	v_mul_f32_e32 v172, v55, v172
	v_cvt_pk_bf16_f32 v166, v165, v166
	v_cvt_pk_bf16_f32 v167, v167, v168
	v_cvt_pk_bf16_f32 v168, v169, v172
	v_cvt_pk_bf16_f32 v169, v170, v171
	v_lshl_add_u64 v[172:173], v[160:161], 0, s[40:41]
	global_store_dwordx4 v[174:175], v[166:169], off
	v_lshl_add_u64 v[176:177], s[12:13], 0, v[172:173]
	v_lshl_add_u64 v[176:177], v[176:177], 0, v[2:3]
	v_lshl_add_u64 v[172:173], s[10:11], 0, v[172:173]
	v_lshl_add_u64 v[172:173], v[172:173], 0, v[158:159]
	v_lshl_add_u64 v[160:161], v[160:161], 0, s[42:43]
	s_waitcnt vmcnt(15)
	v_mov_b32_e32 v170, v202
	v_mov_b32_e32 v171, v203
	v_cvt_pk_f32_fp8_e32 v[166:167], v170
	v_cvt_pk_f32_fp8_sdwa v[168:169], v170 src0_sel:WORD_1
	v_cvt_pk_f32_fp8_e32 v[178:179], v171
	v_cvt_pk_f32_fp8_sdwa v[170:171], v171 src0_sel:WORD_1
	v_mul_f32_e32 v165, 0x3d800000, v166
	v_mul_f32_e32 v166, 0x3d800000, v167
	v_mul_f32_e32 v167, 0x3d800000, v168
	v_mul_f32_e32 v168, 0x3d800000, v169
	v_mul_f32_e32 v169, 0x3d800000, v178
	v_mul_f32_e32 v170, 0x3d800000, v170
	v_mul_f32_e32 v171, 0x3d800000, v171
	v_mul_f32_e32 v178, 0x3d800000, v179
	v_mul_f32_e32 v166, 0xbfb8aa3b, v166
	v_mul_f32_e32 v167, 0xbfb8aa3b, v167
	v_mul_f32_e32 v168, 0xbfb8aa3b, v168
	v_mul_f32_e32 v169, 0xbfb8aa3b, v169
	v_mul_f32_e32 v170, 0xbfb8aa3b, v170
	v_mul_f32_e32 v171, 0xbfb8aa3b, v171
	v_mul_f32_e32 v165, 0xbfb8aa3b, v165
	v_mul_f32_e32 v178, 0xbfb8aa3b, v178
	v_exp_f32_e32 v166, v166
	v_exp_f32_e32 v167, v167
	v_exp_f32_e32 v168, v168
	v_exp_f32_e32 v169, v169
	v_exp_f32_e32 v170, v170
	v_exp_f32_e32 v171, v171
	v_exp_f32_e32 v165, v165
	v_exp_f32_e32 v178, v178
	v_add_f32_e32 v166, 1.0, v166
	v_add_f32_e32 v167, 1.0, v167
	v_add_f32_e32 v168, 1.0, v168
	v_add_f32_e32 v169, 1.0, v169
	v_add_f32_e32 v170, 1.0, v170
	v_add_f32_e32 v171, 1.0, v171
	v_add_f32_e32 v165, 1.0, v165
	v_add_f32_e32 v178, 1.0, v178
	v_rcp_f32_e32 v166, v166
	v_rcp_f32_e32 v167, v167
	v_rcp_f32_e32 v168, v168
	v_rcp_f32_e32 v169, v169
	v_rcp_f32_e32 v170, v170
	v_rcp_f32_e32 v171, v171
	v_rcp_f32_e32 v165, v165
	v_rcp_f32_e32 v178, v178
	v_mul_f32_e32 v166, v27, v166
	v_mul_f32_e32 v167, v28, v167
	v_mul_f32_e32 v168, v29, v168
	v_mul_f32_e32 v169, v22, v169
	v_mul_f32_e32 v170, v24, v170
	v_mul_f32_e32 v171, v25, v171
	v_mul_f32_e32 v165, v26, v165
	v_mul_f32_e32 v178, v23, v178
	v_cvt_pk_bf16_f32 v166, v165, v166
	v_cvt_pk_bf16_f32 v167, v167, v168
	v_cvt_pk_bf16_f32 v168, v169, v178
	v_cvt_pk_bf16_f32 v169, v170, v171
	s_nop 0
	global_store_dwordx4 v[174:175], v[166:169], off offset:256
	s_waitcnt vmcnt(15)
	v_mov_b32_e32 v170, v204
	v_mov_b32_e32 v171, v205
	v_cvt_pk_f32_fp8_e32 v[174:175], v171
	v_cvt_pk_f32_fp8_e32 v[166:167], v170
	v_cvt_pk_f32_fp8_sdwa v[168:169], v170 src0_sel:WORD_1
	v_cvt_pk_f32_fp8_sdwa v[170:171], v171 src0_sel:WORD_1
	v_mul_f32_e32 v165, 0x3d800000, v166
	v_mul_f32_e32 v166, 0x3d800000, v167
	v_mul_f32_e32 v167, 0x3d800000, v168
	v_mul_f32_e32 v168, 0x3d800000, v169
	v_mul_f32_e32 v169, 0x3d800000, v174
	v_mul_f32_e32 v170, 0x3d800000, v170
	v_mul_f32_e32 v171, 0x3d800000, v171
	v_mul_f32_e32 v174, 0x3d800000, v175
	v_mul_f32_e32 v166, 0xbfb8aa3b, v166
	v_mul_f32_e32 v167, 0xbfb8aa3b, v167
	v_mul_f32_e32 v168, 0xbfb8aa3b, v168
	v_mul_f32_e32 v169, 0xbfb8aa3b, v169
	v_mul_f32_e32 v170, 0xbfb8aa3b, v170
	v_mul_f32_e32 v171, 0xbfb8aa3b, v171
	v_mul_f32_e32 v165, 0xbfb8aa3b, v165
	v_mul_f32_e32 v174, 0xbfb8aa3b, v174
	v_exp_f32_e32 v166, v166
	v_exp_f32_e32 v167, v167
	v_exp_f32_e32 v168, v168
	v_exp_f32_e32 v169, v169
	v_exp_f32_e32 v170, v170
	v_exp_f32_e32 v171, v171
	v_exp_f32_e32 v165, v165
	v_exp_f32_e32 v174, v174
	v_add_f32_e32 v166, 1.0, v166
	v_add_f32_e32 v167, 1.0, v167
	v_add_f32_e32 v168, 1.0, v168
	v_add_f32_e32 v169, 1.0, v169
	v_add_f32_e32 v170, 1.0, v170
	v_add_f32_e32 v171, 1.0, v171
	v_add_f32_e32 v165, 1.0, v165
	v_add_f32_e32 v174, 1.0, v174
	v_rcp_f32_e32 v166, v166
	v_rcp_f32_e32 v167, v167
	v_rcp_f32_e32 v168, v168
	v_rcp_f32_e32 v169, v169
	v_rcp_f32_e32 v170, v170
	v_rcp_f32_e32 v171, v171
	v_rcp_f32_e32 v165, v165
	v_rcp_f32_e32 v174, v174
	v_mul_f32_e32 v166, v51, v166
	v_mul_f32_e32 v167, v52, v167
	v_mul_f32_e32 v168, v53, v168
	v_mul_f32_e32 v169, v46, v169
	v_mul_f32_e32 v170, v48, v170
	v_mul_f32_e32 v171, v49, v171
	v_mul_f32_e32 v165, v50, v165
	v_mul_f32_e32 v174, v47, v174
	v_cvt_pk_bf16_f32 v166, v165, v166
	v_cvt_pk_bf16_f32 v167, v167, v168
	v_cvt_pk_bf16_f32 v168, v169, v174
	v_cvt_pk_bf16_f32 v169, v170, v171
	v_lshl_add_u64 v[174:175], s[12:13], 0, v[160:161]
	global_store_dwordx4 v[172:173], v[166:169], off
	v_lshl_add_u64 v[174:175], v[174:175], 0, v[2:3]
	v_lshl_add_u64 v[160:161], s[10:11], 0, v[160:161]
	s_waitcnt vmcnt(15)
	v_mov_b32_e32 v170, v206
	v_mov_b32_e32 v171, v207
	v_cvt_pk_f32_fp8_e32 v[166:167], v170
	v_cvt_pk_f32_fp8_sdwa v[168:169], v170 src0_sel:WORD_1
	v_cvt_pk_f32_fp8_e32 v[176:177], v171
	v_cvt_pk_f32_fp8_sdwa v[170:171], v171 src0_sel:WORD_1
	v_mul_f32_e32 v165, 0x3d800000, v166
	v_mul_f32_e32 v166, 0x3d800000, v167
	v_mul_f32_e32 v167, 0x3d800000, v168
	v_mul_f32_e32 v168, 0x3d800000, v169
	v_mul_f32_e32 v169, 0x3d800000, v176
	v_mul_f32_e32 v170, 0x3d800000, v170
	v_mul_f32_e32 v171, 0x3d800000, v171
	v_mul_f32_e32 v176, 0x3d800000, v177
	v_mul_f32_e32 v166, 0xbfb8aa3b, v166
	v_mul_f32_e32 v167, 0xbfb8aa3b, v167
	v_mul_f32_e32 v168, 0xbfb8aa3b, v168
	v_mul_f32_e32 v169, 0xbfb8aa3b, v169
	v_mul_f32_e32 v170, 0xbfb8aa3b, v170
	v_mul_f32_e32 v171, 0xbfb8aa3b, v171
	v_mul_f32_e32 v165, 0xbfb8aa3b, v165
	v_mul_f32_e32 v176, 0xbfb8aa3b, v176
	v_exp_f32_e32 v166, v166
	v_exp_f32_e32 v167, v167
	v_exp_f32_e32 v168, v168
	v_exp_f32_e32 v169, v169
	v_exp_f32_e32 v170, v170
	v_exp_f32_e32 v171, v171
	v_exp_f32_e32 v165, v165
	v_exp_f32_e32 v176, v176
	v_add_f32_e32 v166, 1.0, v166
	v_add_f32_e32 v167, 1.0, v167
	v_add_f32_e32 v168, 1.0, v168
	v_add_f32_e32 v169, 1.0, v169
	v_add_f32_e32 v170, 1.0, v170
	v_add_f32_e32 v171, 1.0, v171
	v_add_f32_e32 v165, 1.0, v165
	v_add_f32_e32 v176, 1.0, v176
	v_rcp_f32_e32 v166, v166
	v_rcp_f32_e32 v167, v167
	v_rcp_f32_e32 v168, v168
	v_rcp_f32_e32 v169, v169
	v_rcp_f32_e32 v170, v170
	v_rcp_f32_e32 v171, v171
	v_rcp_f32_e32 v165, v165
	v_rcp_f32_e32 v176, v176
	v_mul_f32_e32 v166, v19, v166
	v_mul_f32_e32 v167, v20, v167
	v_mul_f32_e32 v168, v21, v168
	v_mul_f32_e32 v169, v14, v169
	v_mul_f32_e32 v170, v16, v170
	v_mul_f32_e32 v171, v17, v171
	v_mul_f32_e32 v165, v18, v165
	v_mul_f32_e32 v176, v15, v176
	v_cvt_pk_bf16_f32 v166, v165, v166
	v_cvt_pk_bf16_f32 v167, v167, v168
	v_cvt_pk_bf16_f32 v168, v169, v176
	v_cvt_pk_bf16_f32 v169, v170, v171
	s_nop 0
	global_store_dwordx4 v[172:173], v[166:169], off offset:256
	s_waitcnt vmcnt(15)
	v_mov_b32_e32 v170, v208
	v_mov_b32_e32 v171, v209
	v_cvt_pk_f32_fp8_e32 v[172:173], v171
	v_cvt_pk_f32_fp8_e32 v[166:167], v170
	v_cvt_pk_f32_fp8_sdwa v[168:169], v170 src0_sel:WORD_1
	v_cvt_pk_f32_fp8_sdwa v[170:171], v171 src0_sel:WORD_1
	v_mul_f32_e32 v165, 0x3d800000, v166
	v_mul_f32_e32 v166, 0x3d800000, v167
	v_mul_f32_e32 v167, 0x3d800000, v168
	v_mul_f32_e32 v168, 0x3d800000, v169
	v_mul_f32_e32 v169, 0x3d800000, v172
	v_mul_f32_e32 v170, 0x3d800000, v170
	v_mul_f32_e32 v171, 0x3d800000, v171
	v_mul_f32_e32 v172, 0x3d800000, v173
	v_mul_f32_e32 v166, 0xbfb8aa3b, v166
	v_mul_f32_e32 v167, 0xbfb8aa3b, v167
	v_mul_f32_e32 v168, 0xbfb8aa3b, v168
	v_mul_f32_e32 v169, 0xbfb8aa3b, v169
	v_mul_f32_e32 v170, 0xbfb8aa3b, v170
	v_mul_f32_e32 v171, 0xbfb8aa3b, v171
	v_mul_f32_e32 v165, 0xbfb8aa3b, v165
	v_mul_f32_e32 v172, 0xbfb8aa3b, v172
	v_exp_f32_e32 v166, v166
	v_exp_f32_e32 v167, v167
	v_exp_f32_e32 v168, v168
	v_exp_f32_e32 v169, v169
	v_exp_f32_e32 v170, v170
	v_exp_f32_e32 v171, v171
	v_exp_f32_e32 v165, v165
	v_exp_f32_e32 v172, v172
	v_add_f32_e32 v166, 1.0, v166
	v_add_f32_e32 v167, 1.0, v167
	v_add_f32_e32 v168, 1.0, v168
	v_add_f32_e32 v169, 1.0, v169
	v_add_f32_e32 v170, 1.0, v170
	v_add_f32_e32 v171, 1.0, v171
	v_add_f32_e32 v165, 1.0, v165
	v_add_f32_e32 v172, 1.0, v172
	v_rcp_f32_e32 v166, v166
	v_rcp_f32_e32 v167, v167
	v_rcp_f32_e32 v168, v168
	v_rcp_f32_e32 v169, v169
	v_rcp_f32_e32 v170, v170
	v_rcp_f32_e32 v171, v171
	v_rcp_f32_e32 v165, v165
	v_rcp_f32_e32 v172, v172
	v_mul_f32_e32 v166, v43, v166
	v_mul_f32_e32 v167, v44, v167
	v_mul_f32_e32 v168, v45, v168
	v_mul_f32_e32 v169, v38, v169
	v_mul_f32_e32 v170, v40, v170
	v_mul_f32_e32 v171, v41, v171
	v_mul_f32_e32 v165, v42, v165
	v_mul_f32_e32 v172, v39, v172
	v_cvt_pk_bf16_f32 v166, v165, v166
	v_cvt_pk_bf16_f32 v167, v167, v168
	v_cvt_pk_bf16_f32 v168, v169, v172
	v_cvt_pk_bf16_f32 v169, v170, v171
	v_lshl_add_u64 v[172:173], v[160:161], 0, v[158:159]
	global_store_dwordx4 v[172:173], v[166:169], off
	s_waitcnt vmcnt(15)
	v_mov_b32_e32 v170, v210
	v_mov_b32_e32 v171, v211
	v_cvt_pk_f32_fp8_e32 v[158:159], v170
	v_cvt_pk_f32_fp8_sdwa v[160:161], v170 src0_sel:WORD_1
	v_cvt_pk_f32_fp8_e32 v[166:167], v171
	v_cvt_pk_f32_fp8_sdwa v[168:169], v171 src0_sel:WORD_1
	v_mul_f32_e32 v158, 0x3d800000, v158
	v_mul_f32_e32 v159, 0x3d800000, v159
	v_mul_f32_e32 v160, 0x3d800000, v160
	v_mul_f32_e32 v161, 0x3d800000, v161
	v_mul_f32_e32 v165, 0x3d800000, v166
	v_mul_f32_e32 v166, 0x3d800000, v167
	v_mul_f32_e32 v167, 0x3d800000, v168
	v_mul_f32_e32 v168, 0x3d800000, v169
	v_mul_f32_e32 v158, 0xbfb8aa3b, v158
	v_mul_f32_e32 v159, 0xbfb8aa3b, v159
	v_mul_f32_e32 v160, 0xbfb8aa3b, v160
	v_mul_f32_e32 v161, 0xbfb8aa3b, v161
	v_mul_f32_e32 v165, 0xbfb8aa3b, v165
	v_mul_f32_e32 v166, 0xbfb8aa3b, v166
	v_mul_f32_e32 v167, 0xbfb8aa3b, v167
	v_mul_f32_e32 v168, 0xbfb8aa3b, v168
	v_exp_f32_e32 v158, v158
	v_exp_f32_e32 v159, v159
	v_exp_f32_e32 v160, v160
	v_exp_f32_e32 v161, v161
	v_exp_f32_e32 v165, v165
	v_exp_f32_e32 v166, v166
	v_exp_f32_e32 v167, v167
	v_exp_f32_e32 v168, v168
	v_add_f32_e32 v158, 1.0, v158
	v_add_f32_e32 v159, 1.0, v159
	v_add_f32_e32 v160, 1.0, v160
	v_add_f32_e32 v161, 1.0, v161
	v_add_f32_e32 v165, 1.0, v165
	v_add_f32_e32 v166, 1.0, v166
	v_add_f32_e32 v167, 1.0, v167
	v_add_f32_e32 v168, 1.0, v168
	v_rcp_f32_e32 v158, v158
	v_rcp_f32_e32 v159, v159
	v_rcp_f32_e32 v160, v160
	v_rcp_f32_e32 v161, v161
	v_rcp_f32_e32 v165, v165
	v_rcp_f32_e32 v166, v166
	v_rcp_f32_e32 v167, v167
	v_rcp_f32_e32 v168, v168
	v_mul_f32_e32 v158, v10, v158
	v_mul_f32_e32 v159, v11, v159
	v_mul_f32_e32 v160, v12, v160
	v_mul_f32_e32 v161, v13, v161
	v_mul_f32_e32 v165, v6, v165
	v_mul_f32_e32 v166, v7, v166
	v_mul_f32_e32 v167, v8, v167
	v_mul_f32_e32 v168, v9, v168
	v_cvt_pk_bf16_f32 v158, v158, v159
	v_cvt_pk_bf16_f32 v159, v160, v161
	v_cvt_pk_bf16_f32 v160, v165, v166
	v_cvt_pk_bf16_f32 v161, v167, v168
	global_store_dwordx4 v[172:173], v[158:161], off offset:256
	s_cbranch_execnz .LBB0_852
